# P5: the 32 16-bit LDS writes per thread paired through a DPP lane exchange into 16 dword writes (same bytes, same addresses)
# baseline (speedup 1.0000x reference)
.Lp5pf_done:
	v_sub_f32_e32 v66, v97, v66
	v_mul_f32_e32 v66, 0x3fb8aa3b, v66
	v_exp_f32_e32 v66, v66
	s_nop 0
	v_add_f32_e32 v66, 1.0, v66
	v_rcp_f32_e32 v97, v66
	v_lshlrev_b32_e32 v66, 16, v160
	v_mul_f32_e32 v66, 0xbfb8aa3b, v66
	v_and_b32_e32 v160, 0xffff0000, v160
	v_exp_f32_e32 v66, v66
	v_mul_f32_e32 v160, 0xbfb8aa3b, v160
	v_exp_f32_e32 v160, v160
	v_sub_f32_e32 v170, 1.0, v97
	v_add_f32_e32 v66, 1.0, v66
	v_rcp_f32_e32 v66, v66
	v_add_f32_e32 v160, 1.0, v160
	v_rcp_f32_e32 v160, v160
	v_fma_f32 v167, v66, v170, v97
	v_log_f32_e32 v161, v167
	v_fma_f32 v165, v160, v170, v97
	v_log_f32_e32 v160, v165
	v_sub_f32_e32 v167, 1.0, v167
	v_add_f32_e32 v166, 0, v161
	v_sub_f32_e32 v165, 1.0, v165
	v_add_f32_e32 v172, v160, v166
	v_lshlrev_b32_e32 v160, 16, v159
	v_mul_f32_e32 v160, 0xbfb8aa3b, v160
	v_and_b32_e32 v159, 0xffff0000, v159
	v_exp_f32_e32 v160, v160
	v_mul_f32_e32 v159, 0xbfb8aa3b, v159
	v_exp_f32_e32 v159, v159
	v_mov_b32_e32 v66, 0
	v_add_f32_e32 v160, 1.0, v160
	v_rcp_f32_e32 v160, v160
	v_add_f32_e32 v159, 1.0, v159
	v_rcp_f32_e32 v159, v159
	v_fma_f32 v163, v160, v170, v97
	v_log_f32_e32 v160, v163
	v_fma_f32 v161, v159, v170, v97
	v_log_f32_e32 v159, v161
	v_sub_f32_e32 v163, 1.0, v163
	v_add_f32_e32 v173, v160, v172
	v_add_f32_e32 v174, v159, v173
	v_lshlrev_b32_e32 v159, 16, v158
	v_mul_f32_e32 v159, 0xbfb8aa3b, v159
	v_exp_f32_e32 v159, v159
	v_and_b32_e32 v158, 0xffff0000, v158
	v_mul_f32_e32 v158, 0xbfb8aa3b, v158
	v_exp_f32_e32 v158, v158
	v_add_f32_e32 v159, 1.0, v159
	v_rcp_f32_e32 v159, v159
	v_add_f32_e32 v158, 1.0, v158
	v_rcp_f32_e32 v158, v158
	v_fma_f32 v160, v159, v170, v97
	v_log_f32_e32 v159, v160
	v_fma_f32 v158, v158, v170, v97
	v_add_f32_e32 v175, v159, v174
	v_log_f32_e32 v159, v158
	s_nop 0
	v_add_f32_e32 v176, v159, v175
	v_lshlrev_b32_e32 v159, 16, v157
	v_mul_f32_e32 v159, 0xbfb8aa3b, v159
	v_exp_f32_e32 v159, v159
	v_and_b32_e32 v157, 0xffff0000, v157
	v_mul_f32_e32 v157, 0xbfb8aa3b, v157
	v_exp_f32_e32 v157, v157
	v_add_f32_e32 v159, 1.0, v159
	v_rcp_f32_e32 v159, v159
	v_add_f32_e32 v157, 1.0, v157
	v_rcp_f32_e32 v157, v157
	v_fma_f32 v159, v159, v170, v97
	v_log_f32_e32 v162, v159
	v_fma_f32 v171, v157, v170, v97
	v_log_f32_e32 v157, v171
	v_add_f32_e32 v177, v162, v176
	v_lshlrev_b32_e32 v162, 16, v156
	v_mul_f32_e32 v162, 0xbfb8aa3b, v162
	v_and_b32_e32 v156, 0xffff0000, v156
	v_exp_f32_e32 v162, v162
	v_mul_f32_e32 v156, 0xbfb8aa3b, v156
	v_exp_f32_e32 v156, v156
	v_add_f32_e32 v157, v157, v177
	v_add_f32_e32 v162, 1.0, v162
	v_rcp_f32_e32 v162, v162
	v_add_f32_e32 v156, 1.0, v156
	v_rcp_f32_e32 v156, v156
	v_fma_f32 v169, v162, v170, v97
	v_log_f32_e32 v162, v169
	v_fma_f32 v168, v156, v170, v97
	v_log_f32_e32 v156, v168
	v_add_f32_e32 v180, v162, v157
	v_add_f32_e32 v181, v156, v180
	v_lshlrev_b32_e32 v156, 16, v155
	v_mul_f32_e32 v156, 0xbfb8aa3b, v156
	v_and_b32_e32 v155, 0xffff0000, v155
	v_exp_f32_e32 v156, v156
	v_mul_f32_e32 v155, 0xbfb8aa3b, v155
	v_exp_f32_e32 v155, v155
	v_add_f32_e32 v156, 1.0, v156
	v_rcp_f32_e32 v156, v156
	v_add_f32_e32 v155, 1.0, v155
	v_rcp_f32_e32 v155, v155
	v_fma_f32 v164, v156, v170, v97
	v_log_f32_e32 v156, v164
	v_fma_f32 v162, v155, v170, v97
	v_log_f32_e32 v155, v162
	v_add_f32_e32 v182, v156, v181
	v_add_f32_e32 v183, v155, v182
	v_lshlrev_b32_e32 v155, 16, v154
	v_mul_f32_e32 v155, 0xbfb8aa3b, v155
	v_exp_f32_e32 v155, v155
	v_and_b32_e32 v154, 0xffff0000, v154
	v_mul_f32_e32 v154, 0xbfb8aa3b, v154
	v_exp_f32_e32 v154, v154
	v_add_f32_e32 v155, 1.0, v155
	v_rcp_f32_e32 v155, v155
	v_add_f32_e32 v154, 1.0, v154
	v_rcp_f32_e32 v154, v154
	v_fma_f32 v156, v155, v170, v97
	v_log_f32_e32 v155, v156
	s_nop 0
	v_add_f32_e32 v184, v155, v183
	v_fma_f32 v155, v154, v170, v97
	v_log_f32_e32 v154, v155
	s_nop 0
	v_add_f32_e32 v185, v154, v184
	v_lshlrev_b32_e32 v154, 16, v153
	v_mul_f32_e32 v154, 0xbfb8aa3b, v154
	v_and_b32_e32 v153, 0xffff0000, v153
	v_exp_f32_e32 v154, v154
	v_mul_f32_e32 v153, 0xbfb8aa3b, v153
	v_exp_f32_e32 v153, v153
	v_add_f32_e32 v154, 1.0, v154
	v_rcp_f32_e32 v154, v154
	v_add_f32_e32 v153, 1.0, v153
	v_rcp_f32_e32 v153, v153
	v_fma_f32 v154, v154, v170, v97
	v_log_f32_e32 v178, v154
	v_fmac_f32_e32 v97, v153, v170
	v_log_f32_e32 v153, v97
	v_add_f32_e32 v186, v178, v185
	v_add_f32_e32 v153, v153, v186
	ds_write_b32 v85, v153
	s_waitcnt lgkmcnt(0)
	s_barrier
	ds_read2st64_b32 v[178:179], v87 offset1:2
	s_waitcnt lgkmcnt(0)
	v_add_f32_e32 v170, 0, v178
	v_cndmask_b32_e64 v170, v170, 0, s[4:5]
	v_add_f32_e32 v178, v179, v170
	v_cndmask_b32_e64 v170, v170, v178, s[6:7]
	ds_read2st64_b32 v[178:179], v87 offset0:4 offset1:6
	s_waitcnt lgkmcnt(0)
	v_add_f32_e32 v178, v178, v170
	v_cndmask_b32_e64 v170, v170, v178, s[8:9]
	v_add_f32_e32 v178, v179, v170
	v_cndmask_b32_e64 v178, v170, v178, s[10:11]
	v_add_f32_e32 v179, v166, v178
	v_add_f32_e32 v187, v172, v178
	v_add_f32_e32 v188, v173, v178
	v_add_f32_e32 v189, v174, v178
	v_add_f32_e32 v192, v178, v175
	v_add_f32_e32 v193, v178, v176
	v_add_f32_e32 v177, v178, v177
	v_add_f32_e32 v176, v178, v157
	v_add_f32_e32 v175, v178, v180
	v_add_f32_e32 v174, v178, v181
	v_add_f32_e32 v173, v178, v182
	v_add_f32_e32 v172, v178, v183
	v_add_f32_e32 v170, v178, v184
	v_add_f32_e32 v166, v178, v185
	v_add_f32_e32 v157, v178, v186
	v_add_f32_e32 v153, v178, v153
	v_lshlrev_b32_e32 v178, 16, v152
	v_mul_f32_e32 v180, 0xbfb8aa3b, v178
	v_exp_f32_e32 v180, v180
	v_and_b32_e32 v152, 0xffff0000, v152
	v_add_f32_e32 v180, 1.0, v180
	v_rcp_f32_e32 v180, v180
	s_nop 0
	v_mul_f32_e32 v178, v180, v178
	v_exp_f32_e32 v180, v179
	v_exp_f32_e64 v179, -v179
	v_mul_f32_e32 v178, v178, v180
	v_mul_f32_e32 v167, v167, v179
	v_and_b32_e32 v203, 1, v0
	v_cmp_ne_u32_e64 s[100:101], 0, v203
	v_mul_u32_u24_e32 v203, 0x110, v203
	v_and_b32_e32 v202, -4, v89
	v_add_u32_e32 v202, v202, v203
	v_cvt_pk_bf16_f32 v178, v178, v75
	v_mov_b32_e32 v194, v178
	v_cvt_pk_bf16_f32 v167, v167, v75
	v_mov_b32_e32 v195, v167
	v_mul_f32_e32 v167, 0xbfb8aa3b, v152
	v_exp_f32_e32 v167, v167
	s_nop 0
	v_add_f32_e32 v167, 1.0, v167
	v_rcp_f32_e32 v167, v167
	s_nop 0
	v_mul_f32_e32 v152, v167, v152
	v_exp_f32_e32 v167, v187
	s_nop 0
	v_mul_f32_e32 v152, v152, v167
	v_exp_f32_e64 v167, -v187
	v_cvt_pk_bf16_f32 v152, v152, v75
	v_cndmask_b32_e64 v196, v152, v194, s[100:101]
	v_cndmask_b32_e64 v197, v194, v152, s[100:101]
	s_nop 1
	v_mov_b32_dpp v198, v196 quad_perm:[1,0,3,2] row_mask:0xf bank_mask:0xf
	v_cndmask_b32_e64 v199, v197, v198, s[100:101]
	v_cndmask_b32_e64 v200, v198, v197, s[100:101]
	v_lshl_or_b32 v201, v200, 16, v199
	ds_write_b32 v202, v201
	v_mul_f32_e32 v165, v165, v167
	v_cvt_pk_bf16_f32 v152, v165, v75
	v_cndmask_b32_e64 v196, v152, v195, s[100:101]
	v_cndmask_b32_e64 v197, v195, v152, s[100:101]
	s_nop 1
	v_mov_b32_dpp v198, v196 quad_perm:[1,0,3,2] row_mask:0xf bank_mask:0xf
	v_cndmask_b32_e64 v199, v197, v198, s[100:101]
	v_cndmask_b32_e64 v200, v198, v197, s[100:101]
	v_lshl_or_b32 v201, v200, 16, v199
	ds_write_b32 v202, v201 offset:17408
	v_lshlrev_b32_e32 v152, 16, v151
	v_mul_f32_e32 v165, 0xbfb8aa3b, v152
	v_exp_f32_e32 v165, v165
	v_and_b32_e32 v151, 0xffff0000, v151
	v_add_f32_e32 v165, 1.0, v165
	v_rcp_f32_e32 v165, v165
	s_nop 0
	v_mul_f32_e32 v152, v165, v152
	v_exp_f32_e32 v165, v188
	s_nop 0
	v_mul_f32_e32 v152, v152, v165
	v_exp_f32_e64 v165, -v188
	v_cvt_pk_bf16_f32 v152, v152, v75
	v_mov_b32_e32 v194, v152
	v_mul_f32_e32 v163, v163, v165
	v_cvt_pk_bf16_f32 v152, v163, v75
	v_mov_b32_e32 v195, v152
	v_mul_f32_e32 v152, 0xbfb8aa3b, v151
	v_exp_f32_e32 v152, v152
	s_nop 0
	v_add_f32_e32 v152, 1.0, v152
	v_rcp_f32_e32 v152, v152
	s_nop 0
	v_mul_f32_e32 v151, v152, v151
	v_exp_f32_e32 v152, v189
	s_nop 0
	v_mul_f32_e32 v151, v151, v152
	v_sub_f32_e32 v152, 1.0, v161
	v_exp_f32_e64 v161, -v189
	v_cvt_pk_bf16_f32 v151, v151, v75
	v_cndmask_b32_e64 v196, v151, v194, s[100:101]
	v_cndmask_b32_e64 v197, v194, v151, s[100:101]
	s_nop 1
	v_mov_b32_dpp v198, v196 quad_perm:[1,0,3,2] row_mask:0xf bank_mask:0xf
	v_cndmask_b32_e64 v199, v197, v198, s[100:101]
	v_cndmask_b32_e64 v200, v198, v197, s[100:101]
	v_lshl_or_b32 v201, v200, 16, v199
	ds_write_b32 v202, v201 offset:544
	v_mul_f32_e32 v152, v152, v161
	v_cvt_pk_bf16_f32 v151, v152, v75
	v_cndmask_b32_e64 v196, v151, v195, s[100:101]
	v_cndmask_b32_e64 v197, v195, v151, s[100:101]
	s_nop 1
	v_mov_b32_dpp v198, v196 quad_perm:[1,0,3,2] row_mask:0xf bank_mask:0xf
	v_cndmask_b32_e64 v199, v197, v198, s[100:101]
	v_cndmask_b32_e64 v200, v198, v197, s[100:101]
	v_lshl_or_b32 v201, v200, 16, v199
	ds_write_b32 v202, v201 offset:17952
	v_lshlrev_b32_e32 v151, 16, v150
	v_mul_f32_e32 v152, 0xbfb8aa3b, v151
	v_exp_f32_e32 v152, v152
	v_and_b32_e32 v150, 0xffff0000, v150
	v_add_f32_e32 v152, 1.0, v152
	v_rcp_f32_e32 v152, v152
	s_nop 0
	v_mul_f32_e32 v151, v152, v151
	v_exp_f32_e32 v152, v192
	s_nop 0
	v_mul_f32_e32 v151, v151, v152
	v_sub_f32_e32 v152, 1.0, v160
	v_exp_f32_e64 v160, -v192
	v_cvt_pk_bf16_f32 v151, v151, v75
	v_mov_b32_e32 v194, v151
	v_mul_f32_e32 v152, v152, v160
	v_cvt_pk_bf16_f32 v151, v152, v75
	v_mov_b32_e32 v195, v151
	v_mul_f32_e32 v151, 0xbfb8aa3b, v150
	v_exp_f32_e32 v151, v151
	v_exp_f32_e64 v152, -v193
	v_add_f32_e32 v151, 1.0, v151
	v_rcp_f32_e32 v151, v151
	s_nop 0
	v_mul_f32_e32 v150, v151, v150
	v_exp_f32_e32 v151, v193
	s_nop 0
	v_mul_f32_e32 v150, v150, v151
	v_sub_f32_e32 v151, 1.0, v158
	v_cvt_pk_bf16_f32 v150, v150, v75
	v_mul_f32_e32 v151, v151, v152
	v_cndmask_b32_e64 v196, v150, v194, s[100:101]
	v_cndmask_b32_e64 v197, v194, v150, s[100:101]
	s_nop 1
	v_mov_b32_dpp v198, v196 quad_perm:[1,0,3,2] row_mask:0xf bank_mask:0xf
	v_cndmask_b32_e64 v199, v197, v198, s[100:101]
	v_cndmask_b32_e64 v200, v198, v197, s[100:101]
	v_lshl_or_b32 v201, v200, 16, v199
	ds_write_b32 v202, v201 offset:1088
	v_cvt_pk_bf16_f32 v150, v151, v75
	v_cndmask_b32_e64 v196, v150, v195, s[100:101]
	v_cndmask_b32_e64 v197, v195, v150, s[100:101]
	s_nop 1
	v_mov_b32_dpp v198, v196 quad_perm:[1,0,3,2] row_mask:0xf bank_mask:0xf
	v_cndmask_b32_e64 v199, v197, v198, s[100:101]
	v_cndmask_b32_e64 v200, v198, v197, s[100:101]
	v_lshl_or_b32 v201, v200, 16, v199
	ds_write_b32 v202, v201 offset:18496
	v_lshlrev_b32_e32 v150, 16, v149
	v_mul_f32_e32 v151, 0xbfb8aa3b, v150
	v_exp_f32_e32 v151, v151
	v_exp_f32_e64 v152, -v177
	v_and_b32_e32 v149, 0xffff0000, v149
	v_add_f32_e32 v151, 1.0, v151
	v_rcp_f32_e32 v151, v151
	s_nop 0
	v_mul_f32_e32 v150, v151, v150
	v_exp_f32_e32 v151, v177
	s_nop 0
	v_mul_f32_e32 v150, v150, v151
	v_sub_f32_e32 v151, 1.0, v159
	v_cvt_pk_bf16_f32 v150, v150, v75
	v_mul_f32_e32 v151, v151, v152
	v_mov_b32_e32 v194, v150
	v_cvt_pk_bf16_f32 v150, v151, v75
	v_mov_b32_e32 v195, v150
	v_mul_f32_e32 v150, 0xbfb8aa3b, v149
	v_exp_f32_e32 v150, v150
	v_exp_f32_e64 v151, -v176
	v_add_f32_e32 v150, 1.0, v150
	v_rcp_f32_e32 v150, v150
	s_nop 0
	v_mul_f32_e32 v149, v150, v149
	v_exp_f32_e32 v150, v176
	s_nop 0
	v_mul_f32_e32 v149, v149, v150
	v_sub_f32_e32 v150, 1.0, v171
	v_cvt_pk_bf16_f32 v149, v149, v75
	v_mul_f32_e32 v150, v150, v151
	v_cndmask_b32_e64 v196, v149, v194, s[100:101]
	v_cndmask_b32_e64 v197, v194, v149, s[100:101]
	s_nop 1
	v_mov_b32_dpp v198, v196 quad_perm:[1,0,3,2] row_mask:0xf bank_mask:0xf
	v_cndmask_b32_e64 v199, v197, v198, s[100:101]
	v_cndmask_b32_e64 v200, v198, v197, s[100:101]
	v_lshl_or_b32 v201, v200, 16, v199
	ds_write_b32 v202, v201 offset:1632
	v_cvt_pk_bf16_f32 v149, v150, v75
	v_cndmask_b32_e64 v196, v149, v195, s[100:101]
	v_cndmask_b32_e64 v197, v195, v149, s[100:101]
	s_nop 1
	v_mov_b32_dpp v198, v196 quad_perm:[1,0,3,2] row_mask:0xf bank_mask:0xf
	v_cndmask_b32_e64 v199, v197, v198, s[100:101]
	v_cndmask_b32_e64 v200, v198, v197, s[100:101]
	v_lshl_or_b32 v201, v200, 16, v199
	ds_write_b32 v202, v201 offset:19040
	v_lshlrev_b32_e32 v149, 16, v148
	v_mul_f32_e32 v150, 0xbfb8aa3b, v149
	v_exp_f32_e32 v150, v150
	v_exp_f32_e64 v151, -v175
	v_and_b32_e32 v148, 0xffff0000, v148
	v_add_f32_e32 v150, 1.0, v150
	v_rcp_f32_e32 v150, v150
	s_nop 0
	v_mul_f32_e32 v149, v150, v149
	v_exp_f32_e32 v150, v175
	s_nop 0
	v_mul_f32_e32 v149, v149, v150
	v_sub_f32_e32 v150, 1.0, v169
	v_cvt_pk_bf16_f32 v149, v149, v75
	v_mul_f32_e32 v150, v150, v151
	v_mov_b32_e32 v194, v149
	v_cvt_pk_bf16_f32 v149, v150, v75
	v_mov_b32_e32 v195, v149
	v_mul_f32_e32 v149, 0xbfb8aa3b, v148
	v_exp_f32_e32 v149, v149
	v_exp_f32_e64 v150, -v174
	v_add_f32_e32 v149, 1.0, v149
	v_rcp_f32_e32 v149, v149
	s_nop 0
	v_mul_f32_e32 v148, v149, v148
	v_exp_f32_e32 v149, v174
	s_nop 0
	v_mul_f32_e32 v148, v148, v149
	v_sub_f32_e32 v149, 1.0, v168
	v_cvt_pk_bf16_f32 v148, v148, v75
	v_mul_f32_e32 v149, v149, v150
	v_cndmask_b32_e64 v196, v148, v194, s[100:101]
	v_cndmask_b32_e64 v197, v194, v148, s[100:101]
	s_nop 1
	v_mov_b32_dpp v198, v196 quad_perm:[1,0,3,2] row_mask:0xf bank_mask:0xf
	v_cndmask_b32_e64 v199, v197, v198, s[100:101]
	v_cndmask_b32_e64 v200, v198, v197, s[100:101]
	v_lshl_or_b32 v201, v200, 16, v199
	ds_write_b32 v202, v201 offset:2176
	v_cvt_pk_bf16_f32 v148, v149, v75
	v_cndmask_b32_e64 v196, v148, v195, s[100:101]
	v_cndmask_b32_e64 v197, v195, v148, s[100:101]
	s_nop 1
	v_mov_b32_dpp v198, v196 quad_perm:[1,0,3,2] row_mask:0xf bank_mask:0xf
	v_cndmask_b32_e64 v199, v197, v198, s[100:101]
	v_cndmask_b32_e64 v200, v198, v197, s[100:101]
	v_lshl_or_b32 v201, v200, 16, v199
	ds_write_b32 v202, v201 offset:19584
	v_lshlrev_b32_e32 v148, 16, v69
	v_mul_f32_e32 v149, 0xbfb8aa3b, v148
	v_exp_f32_e32 v149, v149
	v_exp_f32_e64 v150, -v173
	v_and_b32_e32 v69, 0xffff0000, v69
	v_add_f32_e32 v149, 1.0, v149
	v_rcp_f32_e32 v149, v149
	s_nop 0
	v_mul_f32_e32 v148, v149, v148
	v_exp_f32_e32 v149, v173
	s_nop 0
	v_mul_f32_e32 v148, v148, v149
	v_sub_f32_e32 v149, 1.0, v164
	v_cvt_pk_bf16_f32 v148, v148, v75
	v_mul_f32_e32 v149, v149, v150
	v_mov_b32_e32 v194, v148
	v_cvt_pk_bf16_f32 v148, v149, v75
	v_mov_b32_e32 v195, v148
	v_mul_f32_e32 v148, 0xbfb8aa3b, v69
	v_exp_f32_e32 v148, v148
	v_exp_f32_e64 v149, -v172
	v_add_f32_e32 v148, 1.0, v148
	v_rcp_f32_e32 v148, v148
	s_nop 0
	v_mul_f32_e32 v69, v148, v69
	v_exp_f32_e32 v148, v172
	s_nop 0
	v_mul_f32_e32 v69, v69, v148
	v_sub_f32_e32 v148, 1.0, v162
	v_cvt_pk_bf16_f32 v69, v69, v75
	v_mul_f32_e32 v148, v148, v149
	v_cndmask_b32_e64 v196, v69, v194, s[100:101]
	v_cndmask_b32_e64 v197, v194, v69, s[100:101]
	s_nop 1
	v_mov_b32_dpp v198, v196 quad_perm:[1,0,3,2] row_mask:0xf bank_mask:0xf
	v_cndmask_b32_e64 v199, v197, v198, s[100:101]
	v_cndmask_b32_e64 v200, v198, v197, s[100:101]
	v_lshl_or_b32 v201, v200, 16, v199
	ds_write_b32 v202, v201 offset:2720
	v_cvt_pk_bf16_f32 v69, v148, v75
	v_cndmask_b32_e64 v196, v69, v195, s[100:101]
	v_cndmask_b32_e64 v197, v195, v69, s[100:101]
	s_nop 1
	v_mov_b32_dpp v198, v196 quad_perm:[1,0,3,2] row_mask:0xf bank_mask:0xf
	v_cndmask_b32_e64 v199, v197, v198, s[100:101]
	v_cndmask_b32_e64 v200, v198, v197, s[100:101]
	v_lshl_or_b32 v201, v200, 16, v199
	ds_write_b32 v202, v201 offset:20128
	v_lshlrev_b32_e32 v69, 16, v68
	v_mul_f32_e32 v148, 0xbfb8aa3b, v69
	v_exp_f32_e32 v148, v148
	v_exp_f32_e64 v149, -v170
	v_and_b32_e32 v68, 0xffff0000, v68
	v_add_f32_e32 v148, 1.0, v148
	v_rcp_f32_e32 v148, v148
	s_nop 0
	v_mul_f32_e32 v69, v148, v69
	v_exp_f32_e32 v148, v170
	s_nop 0
	v_mul_f32_e32 v69, v69, v148
	v_sub_f32_e32 v148, 1.0, v156
	v_cvt_pk_bf16_f32 v69, v69, v75
	v_mul_f32_e32 v148, v148, v149
	v_mov_b32_e32 v194, v69
	v_cvt_pk_bf16_f32 v69, v148, v75
	v_mov_b32_e32 v195, v69
	v_mul_f32_e32 v69, 0xbfb8aa3b, v68
	v_exp_f32_e32 v69, v69
	v_exp_f32_e64 v148, -v166
	v_add_f32_e32 v69, 1.0, v69
	v_rcp_f32_e32 v69, v69
	s_nop 0
	v_mul_f32_e32 v68, v69, v68
	v_exp_f32_e32 v69, v166
	s_nop 0
	v_mul_f32_e32 v68, v68, v69
	v_sub_f32_e32 v69, 1.0, v155
	v_cvt_pk_bf16_f32 v68, v68, v75
	v_mul_f32_e32 v69, v69, v148
	v_cndmask_b32_e64 v196, v68, v194, s[100:101]
	v_cndmask_b32_e64 v197, v194, v68, s[100:101]
	s_nop 1
	v_mov_b32_dpp v198, v196 quad_perm:[1,0,3,2] row_mask:0xf bank_mask:0xf
	v_cndmask_b32_e64 v199, v197, v198, s[100:101]
	v_cndmask_b32_e64 v200, v198, v197, s[100:101]
	v_lshl_or_b32 v201, v200, 16, v199
	ds_write_b32 v202, v201 offset:3264
	v_cvt_pk_bf16_f32 v68, v69, v75
	v_cndmask_b32_e64 v196, v68, v195, s[100:101]
	v_cndmask_b32_e64 v197, v195, v68, s[100:101]
	s_nop 1
	v_mov_b32_dpp v198, v196 quad_perm:[1,0,3,2] row_mask:0xf bank_mask:0xf
	v_cndmask_b32_e64 v199, v197, v198, s[100:101]
	v_cndmask_b32_e64 v200, v198, v197, s[100:101]
	v_lshl_or_b32 v201, v200, 16, v199
	ds_write_b32 v202, v201 offset:20672
	v_lshlrev_b32_e32 v68, 16, v67
	v_mul_f32_e32 v69, 0xbfb8aa3b, v68
	v_exp_f32_e32 v69, v69
	v_exp_f32_e64 v148, -v157
	v_and_b32_e32 v67, 0xffff0000, v67
	v_add_f32_e32 v69, 1.0, v69
	v_rcp_f32_e32 v69, v69
	s_nop 0
	v_mul_f32_e32 v68, v69, v68
	v_exp_f32_e32 v69, v157
	s_nop 0
	v_mul_f32_e32 v68, v68, v69
	v_sub_f32_e32 v69, 1.0, v154
	v_cvt_pk_bf16_f32 v68, v68, v75
	v_mul_f32_e32 v69, v69, v148
	v_mov_b32_e32 v194, v68
	v_cvt_pk_bf16_f32 v68, v69, v75
	v_mov_b32_e32 v195, v68
	v_mul_f32_e32 v68, 0xbfb8aa3b, v67
	v_exp_f32_e32 v68, v68
	v_exp_f32_e64 v69, -v153
	v_add_f32_e32 v68, 1.0, v68
	v_rcp_f32_e32 v68, v68
	s_nop 0
	v_mul_f32_e32 v67, v68, v67
	v_exp_f32_e32 v68, v153
	s_nop 0
	v_mul_f32_e32 v67, v67, v68
	v_sub_f32_e32 v68, 1.0, v97
	v_cvt_pk_bf16_f32 v67, v67, v75
	v_mul_f32_e32 v68, v68, v69
	v_cndmask_b32_e64 v196, v67, v194, s[100:101]
	v_cndmask_b32_e64 v197, v194, v67, s[100:101]
	s_nop 1
	v_mov_b32_dpp v198, v196 quad_perm:[1,0,3,2] row_mask:0xf bank_mask:0xf
	v_cndmask_b32_e64 v199, v197, v198, s[100:101]
	v_cndmask_b32_e64 v200, v198, v197, s[100:101]
	v_lshl_or_b32 v201, v200, 16, v199
	ds_write_b32 v202, v201 offset:3808
	v_cvt_pk_bf16_f32 v67, v68, v75
	v_cndmask_b32_e64 v196, v67, v195, s[100:101]
	v_cndmask_b32_e64 v197, v195, v67, s[100:101]
	s_nop 1
	v_mov_b32_dpp v198, v196 quad_perm:[1,0,3,2] row_mask:0xf bank_mask:0xf
	v_cndmask_b32_e64 v199, v197, v198, s[100:101]
	v_cndmask_b32_e64 v200, v198, v197, s[100:101]
	v_lshl_or_b32 v201, v200, 16, v199
	ds_write_b32 v202, v201 offset:21216
	ds_write_b128 v117, v[26:29] offset:34816
	ds_write_b128 v117, v[30:33] offset:34832
	ds_write_b128 v95, v[34:37]
	ds_write_b128 v118, v[38:41] offset:62464
	ds_write_b128 v95, v[42:45] offset:17408
	ds_write_b128 v119, v[46:49] offset:62464
	v_mov_b32_e32 v26, 0
	v_mov_b32_e32 v27, 0
	v_mov_b32_e32 v28, 0
	v_mov_b32_e32 v29, 0
	s_waitcnt lgkmcnt(0)
	s_barrier
	s_cbranch_vccnz .LBB0_528
	ds_read_b128 v[26:29], v120 offset:17408
	ds_read_b128 v[30:33], v109
	s_waitcnt lgkmcnt(0)
	v_mfma_f32_16x16x32_bf16 v[26:29], v[26:29], v[30:33], 0
	ds_read_b128 v[30:33], v120 offset:17472
	ds_read_b128 v[34:37], v109 offset:64
	s_waitcnt lgkmcnt(0)
	v_mfma_f32_16x16x32_bf16 v[26:29], v[30:33], v[34:37], v[26:29]
	ds_read_b128 v[30:33], v120 offset:17536
	ds_read_b128 v[34:37], v109 offset:128
	s_waitcnt lgkmcnt(0)
	v_mfma_f32_16x16x32_bf16 v[26:29], v[30:33], v[34:37], v[26:29]
	ds_read_b128 v[30:33], v120 offset:17600
	ds_read_b128 v[34:37], v109 offset:192
	s_waitcnt lgkmcnt(0)
	v_mfma_f32_16x16x32_bf16 v[26:29], v[30:33], v[34:37], v[26:29]
